# exp_u: first dot of each chain non-accumulating (no accumulator zeroing)
# speedup vs baseline: 1.0672x; 1.0021x over previous
.LBB0_1262:
	s_waitcnt vmcnt(2)
	ds_write2_b32 v44, v26, v27 offset0:16 offset1:80
	ds_read2_b32 v[26:27], v46 offset0:16 offset1:24
	ds_read2_b32 v[28:29], v46 offset0:32 offset1:40
	ds_read2_b32 v[30:31], v46 offset0:48 offset1:56
	ds_read2_b32 v[32:33], v46 offset0:64 offset1:72
	ds_read2_b32 v[34:35], v46 offset0:80 offset1:88
	ds_read2_b32 v[36:37], v46 offset0:96 offset1:104
	ds_read2_b32 v[38:39], v46 offset0:112 offset1:120
	ds_read2_b32 v[40:41], v46 offset0:128 offset1:136
	s_cmp_lg_u32 s38, 15
	s_cselect_b64 s[40:41], -1, 0
	v_mov_b32_e32 v43, s47
	v_cndmask_b32_e64 v42, 0, 1, s[40:41]
	v_lshl_add_u64 v[42:43], v[42:43], 0, s[38:39]
	v_lshl_add_u64 v[42:43], v[42:43], 0, v[20:21]
	v_lshlrev_b64 v[54:55], 9, v[42:43]
	v_lshlrev_b64 v[42:43], 11, v[42:43]
	s_waitcnt lgkmcnt(7)
	v_lshl_add_u32 v70, v26, 7, v49
	v_lshl_add_u32 v71, v27, 7, v49
	s_waitcnt lgkmcnt(6)
	v_lshl_add_u32 v72, v28, 7, v49
	v_lshl_add_u32 v73, v29, 7, v49
	s_waitcnt lgkmcnt(5)
	v_lshl_add_u32 v74, v30, 7, v49
	v_lshl_add_u32 v75, v31, 7, v49
	s_waitcnt lgkmcnt(4)
	v_lshl_add_u32 v76, v32, 7, v49
	v_lshl_add_u32 v77, v33, 7, v49
	s_waitcnt lgkmcnt(3)
	v_lshl_add_u32 v78, v34, 7, v49
	v_lshl_add_u32 v79, v35, 7, v49
	s_waitcnt lgkmcnt(2)
	v_lshl_add_u32 v80, v36, 7, v49
	v_lshl_add_u32 v82, v37, 7, v49
	s_waitcnt lgkmcnt(1)
	v_lshl_add_u32 v86, v38, 7, v49
	v_lshl_add_u32 v90, v39, 7, v49
	s_waitcnt lgkmcnt(0)
	v_lshl_add_u32 v94, v40, 7, v49
	v_lshl_add_u32 v98, v41, 7, v49
	v_lshl_add_u64 v[110:111], v[12:13], 0, v[54:55]
	v_lshl_add_u64 v[26:27], v[22:23], 0, v[42:43]
	buffer_load_dwordx4 v[28:31], v70, s[24:27], 0 offen sc0
	buffer_load_dwordx4 v[32:35], v71, s[24:27], 0 offen sc0
	buffer_load_dwordx4 v[36:39], v72, s[24:27], 0 offen sc0
	buffer_load_dwordx4 v[40:43], v73, s[24:27], 0 offen sc0
	buffer_load_dwordx4 v[54:57], v74, s[24:27], 0 offen sc0
	buffer_load_dwordx4 v[58:61], v75, s[24:27], 0 offen sc0
	buffer_load_dwordx4 v[62:65], v76, s[24:27], 0 offen sc0
	buffer_load_dwordx4 v[66:69], v77, s[24:27], 0 offen sc0
	s_nop 0
	buffer_load_dwordx4 v[70:73], v78, s[24:27], 0 offen sc0
	buffer_load_dwordx4 v[74:77], v79, s[24:27], 0 offen sc0
	s_nop 0
	buffer_load_dwordx4 v[78:81], v80, s[24:27], 0 offen sc0
	s_nop 0
	buffer_load_dwordx4 v[82:85], v82, s[24:27], 0 offen sc0
	s_nop 0
	buffer_load_dwordx4 v[86:89], v86, s[24:27], 0 offen sc0
	s_nop 0
	buffer_load_dwordx4 v[90:93], v90, s[24:27], 0 offen sc0
	s_nop 0
	buffer_load_dwordx4 v[94:97], v94, s[24:27], 0 offen sc0
	s_nop 0
	buffer_load_dwordx4 v[98:101], v98, s[24:27], 0 offen sc0
	s_nop 0
	global_load_dwordx4 v[102:105], v[26:27], off
	global_load_dwordx4 v[106:109], v[26:27], off offset:16
	s_nop 0
	global_load_dword v26, v[110:111], off
	global_load_dword v27, v[110:111], off offset:256
	s_waitcnt vmcnt(16)
	s_waitcnt vmcnt(12)
	s_add_u32 s38, s38, 1
	s_addc_u32 s39, s39, 0
	s_cmp_eq_u32 s38, 16
	s_waitcnt vmcnt(19)
	v_dot8_i32_i4 v10, v28, v6, 0
	v_dot8_i32_i4 v50, v28, v2, 0
	s_waitcnt vmcnt(18)
	v_dot8_i32_i4 v51, v32, v6, 0
	v_dot8_i32_i4 v52, v32, v2, 0
	v_dot8c_i32_i4_e32 v10, v29, v7
	v_dot8c_i32_i4_e32 v50, v29, v3
	s_waitcnt vmcnt(17)
	v_dot8_i32_i4 v53, v36, v6, 0
	v_dot8_i32_i4 v112, v36, v2, 0
	s_waitcnt vmcnt(16)
	v_dot8_i32_i4 v114, v40, v2, 0
	s_waitcnt vmcnt(15)
	v_dot8_i32_i4 v116, v54, v2, 0
	s_waitcnt vmcnt(14)
	v_dot8_i32_i4 v118, v58, v2, 0
	s_waitcnt vmcnt(13)
	v_dot8_i32_i4 v120, v62, v2, 0
	s_waitcnt vmcnt(12)
	v_dot8_i32_i4 v122, v66, v2, 0
	v_dot8c_i32_i4_e32 v51, v33, v7
	v_dot8c_i32_i4_e32 v52, v33, v3
	v_dot8c_i32_i4_e32 v10, v30, v8
	s_waitcnt vmcnt(11)
	v_dot8_i32_i4 v124, v70, v2, 0
	s_waitcnt vmcnt(10)
	v_dot8_i32_i4 v126, v74, v2, 0
	v_dot8c_i32_i4_e32 v50, v30, v4
	v_dot8_i32_i4 v113, v40, v6, 0
	s_waitcnt vmcnt(9)
	v_dot8_i32_i4 v128, v78, v2, 0
	s_waitcnt vmcnt(8)
	v_dot8_i32_i4 v130, v82, v2, 0
	s_waitcnt vmcnt(7)
	v_dot8_i32_i4 v132, v86, v2, 0
	s_waitcnt vmcnt(6)
	v_dot8_i32_i4 v134, v90, v2, 0
	s_waitcnt vmcnt(5)
	v_dot8_i32_i4 v136, v94, v2, 0
	s_waitcnt vmcnt(4)
	v_dot8_i32_i4 v138, v98, v2, 0
	v_dot8c_i32_i4_e32 v53, v37, v7
	v_dot8c_i32_i4_e32 v112, v37, v3
	v_dot8c_i32_i4_e32 v114, v41, v3
	v_dot8c_i32_i4_e32 v116, v55, v3
	v_dot8c_i32_i4_e32 v118, v59, v3
	v_dot8c_i32_i4_e32 v120, v63, v3
	v_dot8c_i32_i4_e32 v122, v67, v3
	v_dot8c_i32_i4_e32 v124, v71, v3
	v_dot8c_i32_i4_e32 v126, v75, v3
	v_dot8c_i32_i4_e32 v128, v79, v3
	v_dot8c_i32_i4_e32 v130, v83, v3
	v_dot8c_i32_i4_e32 v132, v87, v3
	v_dot8c_i32_i4_e32 v134, v91, v3
	v_dot8c_i32_i4_e32 v136, v95, v3
	v_dot8c_i32_i4_e32 v138, v99, v3
	v_dot8c_i32_i4_e32 v51, v34, v8
	v_dot8c_i32_i4_e32 v52, v34, v4
	v_dot8c_i32_i4_e32 v10, v31, v9
	v_dot8c_i32_i4_e32 v50, v31, v5
	v_dot8_i32_i4 v115, v54, v6, 0
	v_dot8_i32_i4 v123, v70, v6, 0
	v_dot8c_i32_i4_e32 v113, v41, v7
	v_dot8c_i32_i4_e32 v53, v38, v8
	v_dot8c_i32_i4_e32 v112, v38, v4
	v_dot8c_i32_i4_e32 v114, v42, v4
	v_dot8c_i32_i4_e32 v116, v56, v4
	v_dot8c_i32_i4_e32 v118, v60, v4
	v_dot8c_i32_i4_e32 v120, v64, v4
	v_dot8c_i32_i4_e32 v122, v68, v4
	v_dot8c_i32_i4_e32 v124, v72, v4
	v_dot8c_i32_i4_e32 v126, v76, v4
	v_dot8c_i32_i4_e32 v128, v80, v4
	v_dot8c_i32_i4_e32 v130, v84, v4
	v_dot8c_i32_i4_e32 v132, v88, v4
	v_dot8c_i32_i4_e32 v134, v92, v4
	v_dot8c_i32_i4_e32 v136, v96, v4
	v_dot8c_i32_i4_e32 v138, v100, v4
	v_dot8c_i32_i4_e32 v51, v35, v9
	v_dot8c_i32_i4_e32 v52, v35, v5
	v_lshl_add_u32 v4, v10, 4, v50
	v_dot8_i32_i4 v117, v58, v6, 0
	v_dot8_i32_i4 v125, v74, v6, 0
	v_dot8c_i32_i4_e32 v115, v55, v7
	v_dot8c_i32_i4_e32 v123, v71, v7
	v_dot8c_i32_i4_e32 v113, v42, v8
	v_dot8c_i32_i4_e32 v53, v39, v9
	v_dot8c_i32_i4_e32 v112, v39, v5
	v_dot8c_i32_i4_e32 v114, v43, v5
	v_dot8c_i32_i4_e32 v116, v57, v5
	v_dot8c_i32_i4_e32 v118, v61, v5
	v_dot8c_i32_i4_e32 v120, v65, v5
	v_dot8c_i32_i4_e32 v122, v69, v5
	v_dot8c_i32_i4_e32 v124, v73, v5
	v_dot8c_i32_i4_e32 v126, v77, v5
	v_dot8c_i32_i4_e32 v128, v81, v5
	v_dot8c_i32_i4_e32 v130, v85, v5
	v_dot8c_i32_i4_e32 v132, v89, v5
	v_dot8c_i32_i4_e32 v134, v93, v5
	v_dot8c_i32_i4_e32 v136, v97, v5
	v_dot8c_i32_i4_e32 v138, v101, v5
	v_lshl_add_u32 v5, v51, 4, v52
	v_add_u32_dpp v4, v4, v4 quad_perm:[1,0,3,2] row_mask:0xf bank_mask:0xf bound_ctrl:1
	v_dot8_i32_i4 v119, v62, v6, 0
	v_dot8_i32_i4 v127, v78, v6, 0
	v_dot8c_i32_i4_e32 v117, v59, v7
	v_dot8c_i32_i4_e32 v125, v75, v7
	v_dot8c_i32_i4_e32 v115, v56, v8
	v_dot8c_i32_i4_e32 v123, v72, v8
	v_dot8c_i32_i4_e32 v113, v43, v9
	v_lshl_add_u32 v10, v53, 4, v112
	v_add_u32_dpp v5, v5, v5 quad_perm:[1,0,3,2] row_mask:0xf bank_mask:0xf bound_ctrl:1
	v_add_u32_dpp v4, v4, v4 quad_perm:[2,3,0,1] row_mask:0xf bank_mask:0xf bound_ctrl:1
	v_dot8_i32_i4 v121, v66, v6, 0
	v_dot8_i32_i4 v129, v82, v6, 0
	v_dot8c_i32_i4_e32 v119, v63, v7
	v_dot8c_i32_i4_e32 v127, v79, v7
	v_dot8c_i32_i4_e32 v117, v60, v8
	v_dot8c_i32_i4_e32 v125, v76, v8
	v_dot8c_i32_i4_e32 v115, v57, v9
	v_dot8c_i32_i4_e32 v123, v73, v9
	v_lshl_add_u32 v28, v113, 4, v114
	v_add_u32_dpp v10, v10, v10 quad_perm:[1,0,3,2] row_mask:0xf bank_mask:0xf bound_ctrl:1
	v_add_u32_dpp v5, v5, v5 quad_perm:[2,3,0,1] row_mask:0xf bank_mask:0xf bound_ctrl:1
	v_add_u32_dpp v4, v4, v4 row_half_mirror row_mask:0xf bank_mask:0xf bound_ctrl:1
	v_dot8_i32_i4 v131, v86, v6, 0
	v_dot8c_i32_i4_e32 v121, v67, v7
	v_dot8c_i32_i4_e32 v129, v83, v7
	v_dot8c_i32_i4_e32 v119, v64, v8
	v_dot8c_i32_i4_e32 v127, v80, v8
	v_dot8c_i32_i4_e32 v117, v61, v9
	v_dot8c_i32_i4_e32 v125, v77, v9
	v_lshl_add_u32 v29, v115, 4, v116
	v_lshl_add_u32 v33, v123, 4, v124
	v_add_u32_dpp v28, v28, v28 quad_perm:[1,0,3,2] row_mask:0xf bank_mask:0xf bound_ctrl:1
	v_add_u32_dpp v10, v10, v10 quad_perm:[2,3,0,1] row_mask:0xf bank_mask:0xf bound_ctrl:1
	v_add_u32_dpp v5, v5, v5 row_half_mirror row_mask:0xf bank_mask:0xf bound_ctrl:1
	v_cndmask_b32_e64 v4, 0, v4, s[8:9]
	v_dot8_i32_i4 v133, v90, v6, 0
	v_dot8c_i32_i4_e32 v131, v87, v7
	v_dot8c_i32_i4_e32 v121, v68, v8
	v_dot8c_i32_i4_e32 v129, v84, v8
	v_dot8c_i32_i4_e32 v119, v65, v9
	v_dot8c_i32_i4_e32 v127, v81, v9
	v_lshl_add_u32 v30, v117, 4, v118
	v_lshl_add_u32 v34, v125, 4, v126
	v_add_u32_dpp v29, v29, v29 quad_perm:[1,0,3,2] row_mask:0xf bank_mask:0xf bound_ctrl:1
	v_add_u32_dpp v33, v33, v33 quad_perm:[1,0,3,2] row_mask:0xf bank_mask:0xf bound_ctrl:1
	v_add_u32_dpp v28, v28, v28 quad_perm:[2,3,0,1] row_mask:0xf bank_mask:0xf bound_ctrl:1
	v_add_u32_dpp v10, v10, v10 row_half_mirror row_mask:0xf bank_mask:0xf bound_ctrl:1
	v_cndmask_b32_e64 v4, v4, v5, s[10:11]
	v_dot8_i32_i4 v135, v94, v6, 0
	v_dot8c_i32_i4_e32 v133, v91, v7
	v_dot8c_i32_i4_e32 v131, v88, v8
	v_dot8c_i32_i4_e32 v121, v69, v9
	v_dot8c_i32_i4_e32 v129, v85, v9
	v_lshl_add_u32 v31, v119, 4, v120
	v_lshl_add_u32 v35, v127, 4, v128
	v_add_u32_dpp v30, v30, v30 quad_perm:[1,0,3,2] row_mask:0xf bank_mask:0xf bound_ctrl:1
	v_add_u32_dpp v34, v34, v34 quad_perm:[1,0,3,2] row_mask:0xf bank_mask:0xf bound_ctrl:1
	v_add_u32_dpp v29, v29, v29 quad_perm:[2,3,0,1] row_mask:0xf bank_mask:0xf bound_ctrl:1
	v_add_u32_dpp v33, v33, v33 quad_perm:[2,3,0,1] row_mask:0xf bank_mask:0xf bound_ctrl:1
	v_add_u32_dpp v28, v28, v28 row_half_mirror row_mask:0xf bank_mask:0xf bound_ctrl:1
	v_cndmask_b32_e64 v4, v4, v10, s[12:13]
	v_dot8_i32_i4 v137, v98, v6, 0
	v_dot8c_i32_i4_e32 v135, v95, v7
	v_dot8c_i32_i4_e32 v133, v92, v8
	v_dot8c_i32_i4_e32 v131, v89, v9
	v_lshl_add_u32 v32, v121, 4, v122
	v_lshl_add_u32 v36, v129, 4, v130
	v_add_u32_dpp v31, v31, v31 quad_perm:[1,0,3,2] row_mask:0xf bank_mask:0xf bound_ctrl:1
	v_add_u32_dpp v35, v35, v35 quad_perm:[1,0,3,2] row_mask:0xf bank_mask:0xf bound_ctrl:1
	v_add_u32_dpp v30, v30, v30 quad_perm:[2,3,0,1] row_mask:0xf bank_mask:0xf bound_ctrl:1
	v_add_u32_dpp v34, v34, v34 quad_perm:[2,3,0,1] row_mask:0xf bank_mask:0xf bound_ctrl:1
	v_add_u32_dpp v29, v29, v29 row_half_mirror row_mask:0xf bank_mask:0xf bound_ctrl:1
	v_add_u32_dpp v33, v33, v33 row_half_mirror row_mask:0xf bank_mask:0xf bound_ctrl:1
	v_cndmask_b32_e64 v4, v4, v28, s[14:15]
	v_dot8c_i32_i4_e32 v137, v99, v7
	v_dot8c_i32_i4_e32 v135, v96, v8
	v_dot8c_i32_i4_e32 v133, v93, v9
	v_lshl_add_u32 v37, v131, 4, v132
	v_add_u32_dpp v32, v32, v32 quad_perm:[1,0,3,2] row_mask:0xf bank_mask:0xf bound_ctrl:1
	v_add_u32_dpp v36, v36, v36 quad_perm:[1,0,3,2] row_mask:0xf bank_mask:0xf bound_ctrl:1
	v_add_u32_dpp v31, v31, v31 quad_perm:[2,3,0,1] row_mask:0xf bank_mask:0xf bound_ctrl:1
	v_add_u32_dpp v35, v35, v35 quad_perm:[2,3,0,1] row_mask:0xf bank_mask:0xf bound_ctrl:1
	v_add_u32_dpp v30, v30, v30 row_half_mirror row_mask:0xf bank_mask:0xf bound_ctrl:1
	v_add_u32_dpp v34, v34, v34 row_half_mirror row_mask:0xf bank_mask:0xf bound_ctrl:1
	v_cndmask_b32_e64 v33, 0, v33, s[8:9]
	v_cndmask_b32_e64 v4, v4, v29, s[16:17]
	v_dot8c_i32_i4_e32 v137, v100, v8
	v_dot8c_i32_i4_e32 v135, v97, v9
	v_lshl_add_u32 v38, v133, 4, v134
	v_add_u32_dpp v37, v37, v37 quad_perm:[1,0,3,2] row_mask:0xf bank_mask:0xf bound_ctrl:1
	v_add_u32_dpp v32, v32, v32 quad_perm:[2,3,0,1] row_mask:0xf bank_mask:0xf bound_ctrl:1
	v_add_u32_dpp v36, v36, v36 quad_perm:[2,3,0,1] row_mask:0xf bank_mask:0xf bound_ctrl:1
	v_add_u32_dpp v31, v31, v31 row_half_mirror row_mask:0xf bank_mask:0xf bound_ctrl:1
	v_add_u32_dpp v35, v35, v35 row_half_mirror row_mask:0xf bank_mask:0xf bound_ctrl:1
	v_cndmask_b32_e64 v5, v33, v34, s[10:11]
	v_cndmask_b32_e64 v4, v4, v30, s[18:19]
	v_dot8c_i32_i4_e32 v137, v101, v9
	v_lshl_add_u32 v39, v135, 4, v136
	v_add_u32_dpp v38, v38, v38 quad_perm:[1,0,3,2] row_mask:0xf bank_mask:0xf bound_ctrl:1
	v_add_u32_dpp v37, v37, v37 quad_perm:[2,3,0,1] row_mask:0xf bank_mask:0xf bound_ctrl:1
	v_add_u32_dpp v32, v32, v32 row_half_mirror row_mask:0xf bank_mask:0xf bound_ctrl:1
	v_add_u32_dpp v36, v36, v36 row_half_mirror row_mask:0xf bank_mask:0xf bound_ctrl:1
	v_cndmask_b32_e64 v5, v5, v35, s[12:13]
	v_cndmask_b32_e64 v4, v4, v31, s[20:21]
	v_lshl_add_u32 v40, v137, 4, v138
	v_add_u32_dpp v39, v39, v39 quad_perm:[1,0,3,2] row_mask:0xf bank_mask:0xf bound_ctrl:1
	v_add_u32_dpp v38, v38, v38 quad_perm:[2,3,0,1] row_mask:0xf bank_mask:0xf bound_ctrl:1
	v_add_u32_dpp v37, v37, v37 row_half_mirror row_mask:0xf bank_mask:0xf bound_ctrl:1
	v_cndmask_b32_e64 v5, v5, v36, s[14:15]
	v_cndmask_b32_e64 v4, v4, v32, s[22:23]
	v_add_u32_dpp v40, v40, v40 quad_perm:[1,0,3,2] row_mask:0xf bank_mask:0xf bound_ctrl:1
	v_add_u32_dpp v39, v39, v39 quad_perm:[2,3,0,1] row_mask:0xf bank_mask:0xf bound_ctrl:1
	v_add_u32_dpp v38, v38, v38 row_half_mirror row_mask:0xf bank_mask:0xf bound_ctrl:1
	v_cndmask_b32_e64 v5, v5, v37, s[16:17]
	v_cvt_f32_i32_e32 v4, v4
	v_add_u32_dpp v40, v40, v40 quad_perm:[2,3,0,1] row_mask:0xf bank_mask:0xf bound_ctrl:1
	v_add_u32_dpp v39, v39, v39 row_half_mirror row_mask:0xf bank_mask:0xf bound_ctrl:1
	v_cndmask_b32_e64 v5, v5, v38, s[18:19]
	v_add_u32_dpp v40, v40, v40 row_half_mirror row_mask:0xf bank_mask:0xf bound_ctrl:1
	v_cndmask_b32_e64 v5, v5, v39, s[20:21]
	v_cndmask_b32_e64 v5, v5, v40, s[22:23]
	v_cvt_f32_i32_e32 v10, v5
	global_store_dword v[24:25], v4, off offset:-256
	s_waitcnt vmcnt(9)
	s_waitcnt vmcnt(5)
	s_waitcnt vmcnt(4)
	v_mov_b64_e32 v[6:7], v[102:103]
	s_waitcnt vmcnt(3)
	v_mov_b64_e32 v[2:3], v[106:107]
	v_mov_b64_e32 v[8:9], v[104:105]
	v_mov_b64_e32 v[4:5], v[108:109]
	global_store_dword v[24:25], v10, off
	v_lshl_add_u64 v[24:25], v[24:25], 0, s[36:37]
	s_cbranch_scc0 .LBB0_1262
	s_branch .LBB0_1250
